# P9: per-expert padding loop reads the expert counts from LDS (parked by thread 0) instead of a serialized global load + vmcnt(0) per expert; stacked on EpiProj specialisation
# speedup vs baseline: 1.0036x; 1.0036x over previous
; __global__ void __launch_bounds__(NWAVES * 64, 2) fwd_kernel(Args a_unused) {
;     ...
;         if (tid == 0) { int acc = 0; for (int e = 0; e < NEXP; ++e) { tb[e] = acc; acc += (int)((ctl[CW_CNT + 16 * e] + 255u) >> 8); } tb[NEXP] = acc; }
;         __syncthreads();
;         for (int i = gtid; i < NTOK * 4; i += NGT) { const int e = rt_e[i], slot = tb[e] * 256 + rt_r[i]; rt_s[i] = slot; slot_rowoff[slot] = (unsigned)(i >> 2) * (unsigned)D; slot_gate[slot] = rt_g[i]; ((float*)(ws + WS_CS + CS_SLOT))[slot] = ((const float*)(ws + WS_CS + CS_ROW))[i >> 2]; }
;         if (vcu == 0) {
;             for (int e = 0; e < NEXP; ++e) { const int cnt = (int)ctl[CW_CNT + 16 * e], s0 = tb[e] * 256 + cnt, s1 = tb[e + 1] * 256;
.LBB0_2151:
	s_cmp_lt_i32 s46, 10
	s_cselect_b64 s[6:7], -1, 0
	s_and_b64 s[6:7], s[6:7], s[4:5]
	s_andn2_b64 vcc, exec, s[6:7]
	s_cbranch_vccnz .LBB0_2181
	s_mov_b64 s[4:5], s[78:79]
	s_waitcnt lgkmcnt(0)
	s_load_dwordx2 s[8:9], s[4:5], 0xc8
	s_and_saveexec_b64 s[4:5], s[40:41]
	s_cbranch_execz .LBB0_2154
	v_mov_b32_e32 v1, 0x8000
	global_load_dword v3, v1, s[48:49]
	global_load_dword v4, v1, s[48:49] offset:64
	global_load_dword v5, v1, s[48:49] offset:128
	global_load_dword v6, v1, s[48:49] offset:192
	global_load_dword v7, v1, s[48:49] offset:256
	global_load_dword v8, v1, s[48:49] offset:320
	global_load_dword v9, v1, s[48:49] offset:384
	global_load_dword v10, v1, s[48:49] offset:448
	global_load_dword v11, v1, s[48:49] offset:512
	global_load_dword v12, v1, s[48:49] offset:576
	global_load_dword v13, v1, s[48:49] offset:640
	global_load_dword v14, v1, s[48:49] offset:704
	global_load_dword v15, v1, s[48:49] offset:768
	global_load_dword v16, v1, s[48:49] offset:832
	global_load_dword v17, v1, s[48:49] offset:896
	global_load_dword v18, v1, s[48:49] offset:960
	global_load_dword v19, v1, s[48:49] offset:1024
	global_load_dword v20, v1, s[48:49] offset:1088
	global_load_dword v21, v1, s[48:49] offset:1152
	global_load_dword v22, v1, s[48:49] offset:1216
	global_load_dword v23, v1, s[48:49] offset:1280
	global_load_dword v24, v1, s[48:49] offset:1344
	global_load_dword v25, v1, s[48:49] offset:1408
	global_load_dword v26, v1, s[48:49] offset:1472
	global_load_dword v27, v1, s[48:49] offset:1536
	global_load_dword v28, v1, s[48:49] offset:1600
	global_load_dword v29, v1, s[48:49] offset:1664
	global_load_dword v30, v1, s[48:49] offset:1728
	global_load_dword v31, v1, s[48:49] offset:1792
	global_load_dword v32, v1, s[48:49] offset:1856
	global_load_dword v33, v1, s[48:49] offset:1920
	global_load_dword v34, v1, s[48:49] offset:1984
	s_waitcnt vmcnt(0)
	v_mov_b32_e32 v2, 0
	ds_write_b32 v2, v3 offset:252
	ds_write_b128 v2, v[4:7] offset:256
	ds_write_b128 v2, v[8:11] offset:272
	ds_write_b128 v2, v[12:15] offset:288
	ds_write_b128 v2, v[16:19] offset:304
	ds_write_b128 v2, v[20:23] offset:320
	ds_write_b128 v2, v[24:27] offset:336
	ds_write_b128 v2, v[28:31] offset:352
	ds_write_b64 v2, v[32:33] offset:368
	ds_write_b32 v2, v34 offset:376
	v_add_u32_e32 v1, 0xff, v3
	v_add_u32_e32 v4, 0xff, v4
	v_add_u32_e32 v5, 0xff, v5
	v_lshrrev_b32_e32 v3, 8, v1
	v_lshrrev_b32_e32 v1, 8, v4
	v_add_u32_e32 v6, 0xff, v6
	v_lshrrev_b32_e32 v5, 8, v5
	v_add_u32_e32 v4, v1, v3
	v_add_u32_e32 v7, 0xff, v7
	v_lshrrev_b32_e32 v6, 8, v6
	v_add_u32_e32 v5, v5, v4
	v_add_u32_e32 v8, 0xff, v8
	v_lshrrev_b32_e32 v7, 8, v7
	ds_write_b128 v2, v[2:5]
	v_add_u32_e32 v4, v6, v5
	v_add_u32_e32 v9, 0xff, v9
	v_lshrrev_b32_e32 v8, 8, v8
	v_add_u32_e32 v5, v7, v4
	v_add_u32_e32 v10, 0xff, v10
	v_lshrrev_b32_e32 v9, 8, v9
	v_add_u32_e32 v6, v8, v5
	v_add_u32_e32 v11, 0xff, v11
	v_lshrrev_b32_e32 v10, 8, v10
	v_add_u32_e32 v7, v9, v6
	v_add_u32_e32 v12, 0xff, v12
	v_lshrrev_b32_e32 v11, 8, v11
	ds_write_b128 v2, v[4:7] offset:16
	v_add_u32_e32 v4, v10, v7
	v_add_u32_e32 v13, 0xff, v13
	v_lshrrev_b32_e32 v12, 8, v12
	v_add_u32_e32 v5, v11, v4
	v_add_u32_e32 v14, 0xff, v14
	v_lshrrev_b32_e32 v13, 8, v13
	v_add_u32_e32 v6, v12, v5
	v_add_u32_e32 v15, 0xff, v15
	v_lshrrev_b32_e32 v14, 8, v14
	v_add_u32_e32 v7, v13, v6
	v_add_u32_e32 v16, 0xff, v16
	v_lshrrev_b32_e32 v15, 8, v15
	ds_write_b128 v2, v[4:7] offset:32
	v_add_u32_e32 v4, v14, v7
	v_add_u32_e32 v17, 0xff, v17
	v_lshrrev_b32_e32 v16, 8, v16
	v_add_u32_e32 v5, v15, v4
	v_add_u32_e32 v18, 0xff, v18
	v_lshrrev_b32_e32 v17, 8, v17
	v_add_u32_e32 v6, v16, v5
	v_add_u32_e32 v19, 0xff, v19
	v_lshrrev_b32_e32 v18, 8, v18
	v_add_u32_e32 v7, v17, v6
	v_add_u32_e32 v20, 0xff, v20
	v_lshrrev_b32_e32 v19, 8, v19
	ds_write_b128 v2, v[4:7] offset:48
	v_add_u32_e32 v4, v18, v7
	v_add_u32_e32 v21, 0xff, v21
	v_lshrrev_b32_e32 v20, 8, v20
	v_add_u32_e32 v5, v19, v4
	v_add_u32_e32 v22, 0xff, v22
	v_lshrrev_b32_e32 v21, 8, v21
	v_add_u32_e32 v6, v20, v5
	v_add_u32_e32 v23, 0xff, v23
	v_lshrrev_b32_e32 v22, 8, v22
	v_add_u32_e32 v7, v21, v6
	v_add_u32_e32 v24, 0xff, v24
	v_lshrrev_b32_e32 v23, 8, v23
	ds_write_b128 v2, v[4:7] offset:64
	v_add_u32_e32 v4, v22, v7
	v_lshrrev_b32_e32 v24, 8, v24
	v_add_u32_e32 v5, v23, v4
	v_add_u32_e32 v1, 0xff, v25
	v_add_u32_e32 v6, v24, v5
	v_lshrrev_b32_e32 v1, 8, v1
	v_add_u32_e32 v7, v1, v6
	v_add_u32_e32 v1, 0xff, v26
	v_lshrrev_b32_e32 v1, 8, v1
	ds_write_b128 v2, v[4:7] offset:80
	v_add_u32_e32 v4, v1, v7
	v_add_u32_e32 v1, 0xff, v27
	v_lshrrev_b32_e32 v1, 8, v1
	v_add_u32_e32 v5, v1, v4
	v_add_u32_e32 v1, 0xff, v28
	v_lshrrev_b32_e32 v1, 8, v1
	v_add_u32_e32 v6, v1, v5
	v_add_u32_e32 v1, 0xff, v29
	v_lshrrev_b32_e32 v1, 8, v1
	v_add_u32_e32 v7, v1, v6
	v_add_u32_e32 v1, 0xff, v30
	v_lshrrev_b32_e32 v1, 8, v1
	ds_write_b128 v2, v[4:7] offset:96
	v_add_u32_e32 v4, v1, v7
	v_add_u32_e32 v1, 0xff, v31
	v_lshrrev_b32_e32 v1, 8, v1
	v_add_u32_e32 v5, v1, v4
	v_add_u32_e32 v1, 0xff, v32
	v_lshrrev_b32_e32 v1, 8, v1
	v_add_u32_e32 v6, v1, v5
	v_add_u32_e32 v1, 0xff, v33
	v_lshrrev_b32_e32 v1, 8, v1
	v_add_u32_e32 v7, v1, v6
	v_add_u32_e32 v1, 0xff, v34
	v_lshrrev_b32_e32 v1, 8, v1
	v_add_u32_e32 v1, v1, v7
	ds_write_b128 v2, v[4:7] offset:112
	ds_write_b32 v2, v1 offset:128

; __global__ void __launch_bounds__(NWAVES * 64, 2) fwd_kernel(Args a_unused) {
;     ...
;             for (int e = 0; e < NEXP; ++e) { const int cnt = (int)ctl[CW_CNT + 16 * e], s0 = tb[e] * 256 + cnt, s1 = tb[e + 1] * 256;
;                 for (int s = s0 + tid; s < s1; s += 512) { slot_rowoff[s] = 0u; slot_gate[s] = 0.f; ((float*)(ws + WS_CS + CS_SLOT))[s] = 0.f; }
.LBB0_2161:
	s_lshl_b32 s4, s27, 2
	s_add_i32 s4, s4, 0
	v_mov_b32_e32 v3, s4
	s_waitcnt lgkmcnt(0)
	v_mov_b32_e32 v10, v9
	ds_read_b32 v9, v3 offset:4
	ds_read_b32 v2, v3 offset:252
	v_lshlrev_b32_e32 v3, 8, v10
	s_waitcnt lgkmcnt(0)
	v_lshlrev_b32_e32 v11, 8, v9
	v_add_u32_e32 v3, v3, v2
	v_add_u32_e32 v2, v3, v0
	v_cmp_lt_i32_e32 vcc, v2, v11
	s_and_saveexec_b64 s[20:21], vcc
	s_cbranch_execz .LBB0_2169
	v_add_u32_e32 v4, v3, v7
	v_max_i32_e32 v4, v11, v4
	v_add_u32_e32 v4, v4, v6
	v_sub_u32_e32 v3, v4, v3
	v_cmp_lt_u32_e32 vcc, s3, v3
	s_mov_b64 s[24:25], -1
	s_and_saveexec_b64 s[22:23], vcc
	s_cbranch_execz .LBB0_2166
	v_lshrrev_b32_e32 v3, 9, v3
	v_add_u32_e32 v12, 1, v3
	v_and_b32_e32 v13, 0xfffffe, v12
	v_add_u32_e32 v3, 0x200, v2
	s_mov_b64 s[24:25], 0
	v_mov_b32_e32 v14, v13
	v_mov_b64_e32 v[4:5], v[2:3]
